# pipelined the serialised residual-load/store ladders in the three EpiResid/EpiResidNorm GEMM epilogues (renamed load destinations into dead registers, counted vmcnt instead of vmcnt(0) per element)
# speedup vs baseline: 1.0157x; 1.0096x over previous
.LBB0_907:
	v_ashrrev_i32_e32 v128, 4, v177
	s_lshl_b32 s0, s10, 8
	v_lshlrev_b32_e32 v178, 2, v128
	s_or_b32 s0, s0, s63
	v_add_u32_e32 v150, s0, v178
	s_ashr_i32 s0, s8, 31
	s_lshr_b32 s0, s0, 29
	s_add_i32 s0, s8, s0
	s_lshl_b32 s6, s8, 8
	s_ashr_i32 s0, s0, 3
	s_mul_hi_i32 s5, s0, 0x3000
	s_mul_i32 s4, s0, 0x3000
	v_add_u32_e32 v166, s6, v176
	v_lshl_add_u64 v[158:159], s[4:5], 2, v[162:163]
	v_ashrrev_i32_e32 v151, 31, v150
	v_ashrrev_i32_e32 v167, 31, v166
	v_lshl_add_u64 v[132:133], v[150:151], 2, v[158:159]
	s_mov_b32 s0, 0x404000
	v_lshlrev_b64 v[152:153], 11, v[166:167]
	v_add_co_u32_e32 v134, vcc, s0, v132
	v_lshl_add_u64 v[128:129], v[152:153], 0, v[150:151]
	v_readlane_b32 s0, v254, 9
	v_lshlrev_b64 v[136:137], 2, v[128:129]
	v_readlane_b32 s1, v254, 10
	s_waitcnt vmcnt(0)
	s_barrier
	v_addc_co_u32_e32 v135, vcc, 0, v133, vcc
	v_lshl_add_u64 v[154:155], s[0:1], 0, v[136:137]
	global_load_dwordx4 v[188:191], v[154:155], off
	global_load_dwordx4 v[144:147], v[134:135], off
	s_mov_b64 s[4:5], 0x404000
	v_lshl_add_u64 v[168:169], v[164:165], 0, v[136:137]
	v_lshl_add_u64 v[132:133], v[132:133], 0, s[4:5]
	global_load_dwordx4 v[140:143], v[132:133], off offset:64
	global_load_dwordx4 v[136:139], v[132:133], off offset:512
	global_load_dwordx4 v[132:135], v[132:133], off offset:576
	global_load_dwordx4 v[192:195], v[154:155], off offset:64
	global_load_dwordx4 v[196:199], v[154:155], off offset:512
	global_load_dwordx4 v[200:203], v[154:155], off offset:576
	s_mov_b64 s[4:5], 0x40000
	s_mov_b64 s[14:15], 0x48000
	s_movk_i32 s9, 0x44
	s_waitcnt vmcnt(6)
	v_pk_fma_f32 v[126:127], v[126:127], v[146:147], v[190:191]
	v_pk_fma_f32 v[124:125], v[124:125], v[144:145], v[188:189]
	global_store_dwordx4 v[168:169], v[124:127], off
	s_waitcnt vmcnt(3)
	v_pk_fma_f32 v[122:123], v[122:123], v[142:143], v[194:195]
	v_pk_fma_f32 v[120:121], v[120:121], v[140:141], v[192:193]
	global_store_dwordx4 v[168:169], v[120:123], off offset:64
	s_waitcnt vmcnt(3)
	v_pk_fma_f32 v[118:119], v[118:119], v[138:139], v[198:199]
	v_pk_fma_f32 v[116:117], v[116:117], v[136:137], v[196:197]
	global_store_dwordx4 v[168:169], v[116:119], off offset:512
	v_or_b32_e32 v154, 16, v166
	v_ashrrev_i32_e32 v155, 31, v154
	v_lshlrev_b64 v[156:157], 11, v[154:155]
	v_lshl_add_u64 v[154:155], v[156:157], 0, v[150:151]
	v_lshlrev_b64 v[154:155], 2, v[154:155]
	v_lshl_add_u64 v[170:171], s[0:1], 0, v[154:155]
	global_load_dwordx4 v[204:207], v[170:171], off
	global_load_dwordx4 v[208:211], v[170:171], off offset:64
	global_load_dwordx4 v[212:215], v[170:171], off offset:512
	global_load_dwordx4 v[216:219], v[170:171], off offset:576
	s_waitcnt vmcnt(7)
	v_pk_fma_f32 v[130:131], v[106:107], v[134:135], v[202:203]
	v_pk_fma_f32 v[128:129], v[104:105], v[132:133], v[200:201]
	global_store_dwordx4 v[168:169], v[128:131], off offset:576
	v_lshl_add_u64 v[168:169], v[164:165], 0, v[154:155]
	v_or_b32_e32 v154, 32, v166
	v_ashrrev_i32_e32 v155, 31, v154
	v_lshlrev_b64 v[154:155], 11, v[154:155]
	v_or_b32_e32 v166, 48, v166
	v_ashrrev_i32_e32 v167, 31, v166
	v_lshlrev_b64 v[166:167], 11, v[166:167]
	s_waitcnt vmcnt(4)
	v_pk_fma_f32 v[114:115], v[114:115], v[146:147], v[206:207]
	v_pk_fma_f32 v[112:113], v[112:113], v[144:145], v[204:205]
	global_store_dwordx4 v[168:169], v[112:115], off
	s_waitcnt vmcnt(4)
	v_pk_fma_f32 v[106:107], v[110:111], v[142:143], v[210:211]
	v_pk_fma_f32 v[104:105], v[108:109], v[140:141], v[208:209]
	global_store_dwordx4 v[168:169], v[104:107], off offset:64
	s_waitcnt vmcnt(4)
	v_pk_fma_f32 v[102:103], v[102:103], v[138:139], v[214:215]
	v_pk_fma_f32 v[100:101], v[100:101], v[136:137], v[212:213]
	global_store_dwordx4 v[168:169], v[100:103], off offset:512
	v_lshl_add_u64 v[170:171], v[154:155], 0, v[150:151]
	v_lshlrev_b64 v[170:171], 2, v[170:171]
	v_lshl_add_u64 v[172:173], s[0:1], 0, v[170:171]
	global_load_dwordx4 v[220:223], v[172:173], off
	global_load_dwordx4 v[224:227], v[172:173], off offset:64
	global_load_dwordx4 v[228:231], v[172:173], off offset:512
	global_load_dwordx4 v[232:235], v[172:173], off offset:576
	s_waitcnt vmcnt(8)
	v_pk_fma_f32 v[110:111], v[90:91], v[134:135], v[218:219]
	v_pk_fma_f32 v[108:109], v[88:89], v[132:133], v[216:217]
	global_store_dwordx4 v[168:169], v[108:111], off offset:576
	v_lshl_add_u64 v[168:169], v[164:165], 0, v[170:171]
	v_lshl_add_u64 v[170:171], v[166:167], 0, v[150:151]
	v_lshlrev_b64 v[170:171], 2, v[170:171]
	s_waitcnt vmcnt(4)
	v_pk_fma_f32 v[90:91], v[98:99], v[146:147], v[222:223]
	v_pk_fma_f32 v[88:89], v[96:97], v[144:145], v[220:221]
	global_store_dwordx4 v[168:169], v[88:91], off
	s_waitcnt vmcnt(4)
	v_pk_fma_f32 v[94:95], v[94:95], v[142:143], v[226:227]
	v_pk_fma_f32 v[92:93], v[92:93], v[140:141], v[224:225]
	global_store_dwordx4 v[168:169], v[92:95], off offset:64
	s_waitcnt vmcnt(4)
	v_pk_fma_f32 v[86:87], v[86:87], v[138:139], v[230:231]
	v_pk_fma_f32 v[84:85], v[84:85], v[136:137], v[228:229]
	global_store_dwordx4 v[168:169], v[84:87], off offset:512
	v_lshl_add_u64 v[172:173], s[0:1], 0, v[170:171]
	global_load_dwordx4 v[188:191], v[172:173], off
	global_load_dwordx4 v[192:195], v[172:173], off offset:64
	global_load_dwordx4 v[196:199], v[172:173], off offset:512
	global_load_dwordx4 v[200:203], v[172:173], off offset:576
	v_lshl_add_u64 v[170:171], v[164:165], 0, v[170:171]
	s_waitcnt vmcnt(8)
	v_pk_fma_f32 v[74:75], v[74:75], v[134:135], v[234:235]
	v_pk_fma_f32 v[72:73], v[72:73], v[132:133], v[232:233]
	global_store_dwordx4 v[168:169], v[72:75], off offset:576
	v_lshl_add_u64 v[168:169], v[152:153], 0, s[4:5]
	s_waitcnt vmcnt(4)
	v_pk_fma_f32 v[82:83], v[82:83], v[146:147], v[190:191]
	v_pk_fma_f32 v[80:81], v[80:81], v[144:145], v[188:189]
	global_store_dwordx4 v[170:171], v[80:83], off
	s_waitcnt vmcnt(4)
	v_pk_fma_f32 v[78:79], v[78:79], v[142:143], v[194:195]
	v_pk_fma_f32 v[76:77], v[76:77], v[140:141], v[192:193]
	global_store_dwordx4 v[170:171], v[76:79], off offset:64
	s_waitcnt vmcnt(4)
	v_pk_fma_f32 v[70:71], v[70:71], v[138:139], v[198:199]
	v_pk_fma_f32 v[68:69], v[68:69], v[136:137], v[196:197]
	global_store_dwordx4 v[170:171], v[68:71], off offset:512
	v_lshl_add_u64 v[172:173], v[168:169], 0, v[150:151]
	v_lshlrev_b64 v[172:173], 2, v[172:173]
	v_lshl_add_u64 v[174:175], s[0:1], 0, v[172:173]
	global_load_dwordx4 v[204:207], v[174:175], off
	global_load_dwordx4 v[208:211], v[174:175], off offset:64
	global_load_dwordx4 v[212:215], v[174:175], off offset:512
	global_load_dwordx4 v[216:219], v[174:175], off offset:576
	v_lshl_add_u64 v[172:173], v[164:165], 0, v[172:173]
	s_waitcnt vmcnt(8)
	v_pk_fma_f32 v[66:67], v[66:67], v[134:135], v[202:203]
	v_pk_fma_f32 v[64:65], v[64:65], v[132:133], v[200:201]
	global_store_dwordx4 v[170:171], v[64:67], off offset:576
	v_lshl_add_u64 v[170:171], v[152:153], 0, s[14:15]
	s_mov_b64 s[14:15], 0x50000
	s_waitcnt vmcnt(4)
	v_pk_fma_f32 v[62:63], v[62:63], v[146:147], v[206:207]
	v_pk_fma_f32 v[60:61], v[60:61], v[144:145], v[204:205]
	global_store_dwordx4 v[172:173], v[60:63], off
	s_waitcnt vmcnt(4)
	v_pk_fma_f32 v[58:59], v[58:59], v[142:143], v[210:211]
	v_pk_fma_f32 v[56:57], v[56:57], v[140:141], v[208:209]
	global_store_dwordx4 v[172:173], v[56:59], off offset:64
	s_waitcnt vmcnt(4)
	v_pk_fma_f32 v[54:55], v[54:55], v[138:139], v[214:215]
	v_pk_fma_f32 v[52:53], v[52:53], v[136:137], v[212:213]
	global_store_dwordx4 v[172:173], v[52:55], off offset:512
	v_lshl_add_u64 v[174:175], v[170:171], 0, v[150:151]
	v_lshlrev_b64 v[174:175], 2, v[174:175]
	v_lshl_add_u64 v[180:181], s[0:1], 0, v[174:175]
	global_load_dwordx4 v[220:223], v[180:181], off
	global_load_dwordx4 v[224:227], v[180:181], off offset:64
	global_load_dwordx4 v[228:231], v[180:181], off offset:512
	global_load_dwordx4 v[232:235], v[180:181], off offset:576
	v_lshl_add_u64 v[174:175], v[164:165], 0, v[174:175]
	s_waitcnt vmcnt(8)
	v_pk_fma_f32 v[42:43], v[42:43], v[134:135], v[218:219]
	v_pk_fma_f32 v[40:41], v[40:41], v[132:133], v[216:217]
	global_store_dwordx4 v[172:173], v[40:43], off offset:576
	v_lshl_add_u64 v[172:173], v[152:153], 0, s[14:15]
	s_mov_b64 s[14:15], 0x58000
	s_waitcnt vmcnt(4)
	v_pk_fma_f32 v[50:51], v[50:51], v[146:147], v[222:223]
	v_pk_fma_f32 v[48:49], v[48:49], v[144:145], v[220:221]
	global_store_dwordx4 v[174:175], v[48:51], off
	s_waitcnt vmcnt(4)
	v_pk_fma_f32 v[46:47], v[46:47], v[142:143], v[226:227]
	v_pk_fma_f32 v[44:45], v[44:45], v[140:141], v[224:225]
	global_store_dwordx4 v[174:175], v[44:47], off offset:64
	s_waitcnt vmcnt(4)
	v_pk_fma_f32 v[38:39], v[38:39], v[138:139], v[230:231]
	v_pk_fma_f32 v[36:37], v[36:37], v[136:137], v[228:229]
	global_store_dwordx4 v[174:175], v[36:39], off offset:512
	v_lshl_add_u64 v[180:181], v[172:173], 0, v[150:151]
	v_lshlrev_b64 v[180:181], 2, v[180:181]
	v_lshl_add_u64 v[182:183], s[0:1], 0, v[180:181]
	global_load_dwordx4 v[188:191], v[182:183], off
	global_load_dwordx4 v[192:195], v[182:183], off offset:64
	global_load_dwordx4 v[196:199], v[182:183], off offset:512
	global_load_dwordx4 v[200:203], v[182:183], off offset:576
	v_lshl_add_u64 v[180:181], v[164:165], 0, v[180:181]
	s_waitcnt vmcnt(8)
	v_pk_fma_f32 v[98:99], v[26:27], v[134:135], v[234:235]
	v_pk_fma_f32 v[96:97], v[24:25], v[132:133], v[232:233]
	global_store_dwordx4 v[174:175], v[96:99], off offset:576
	v_lshl_add_u64 v[174:175], v[152:153], 0, s[14:15]
	s_waitcnt vmcnt(4)
	v_pk_fma_f32 v[26:27], v[34:35], v[146:147], v[190:191]
	v_pk_fma_f32 v[24:25], v[32:33], v[144:145], v[188:189]
	global_store_dwordx4 v[180:181], v[24:27], off
	s_waitcnt vmcnt(4)
	v_pk_fma_f32 v[30:31], v[30:31], v[142:143], v[194:195]
	v_pk_fma_f32 v[28:29], v[28:29], v[140:141], v[192:193]
	global_store_dwordx4 v[180:181], v[28:31], off offset:64
	s_waitcnt vmcnt(4)
	v_pk_fma_f32 v[22:23], v[22:23], v[138:139], v[198:199]
	v_pk_fma_f32 v[20:21], v[20:21], v[136:137], v[196:197]
	global_store_dwordx4 v[180:181], v[20:23], off offset:512
	v_lshl_add_u64 v[182:183], v[174:175], 0, v[150:151]
	v_lshlrev_b64 v[184:185], 2, v[182:183]
	v_lshl_add_u64 v[186:187], s[0:1], 0, v[184:185]
	global_load_dwordx4 v[204:207], v[186:187], off
	global_load_dwordx4 v[208:211], v[186:187], off offset:64
	global_load_dwordx4 v[212:215], v[186:187], off offset:512
	global_load_dwordx4 v[216:219], v[186:187], off offset:576
	s_lshl_b32 s0, s62, 4
	s_add_i32 s0, s0, 0
	v_readlane_b32 s1, v254, 0
	s_waitcnt vmcnt(8)
	v_pk_fma_f32 v[14:15], v[14:15], v[134:135], v[202:203]
	v_pk_fma_f32 v[12:13], v[12:13], v[132:133], v[200:201]
	global_store_dwordx4 v[180:181], v[12:15], off offset:576
	v_lshl_add_u64 v[34:35], v[164:165], 0, v[184:185]
	v_lshl_add_u64 v[32:33], v[162:163], 0, s[4:5]
	s_waitcnt vmcnt(4)
	v_pk_fma_f32 v[18:19], v[18:19], v[146:147], v[206:207]
	v_pk_fma_f32 v[16:17], v[16:17], v[144:145], v[204:205]
	global_store_dwordx4 v[34:35], v[16:19], off
	v_mul_f32_e32 v146, v125, v125
	v_mul_f32_e32 v147, v127, v127
	v_mul_lo_u32 v145, v176, s9
	v_fmac_f32_e32 v146, v124, v124
	v_fmac_f32_e32 v147, v126, v126
	v_add3_u32 v145, s0, v178, v145
	v_add_f32_e32 v146, v146, v147
	v_mul_f32_e32 v147, v121, v121
	v_mul_f32_e32 v178, v123, v123
	v_fmac_f32_e32 v147, v120, v120
	v_fmac_f32_e32 v178, v122, v122
	v_add_f32_e32 v147, v147, v178
	v_add_f32_e32 v146, v146, v147
	v_mul_f32_e32 v147, v117, v117
	v_mul_f32_e32 v178, v119, v119
	v_fmac_f32_e32 v147, v116, v116
	v_fmac_f32_e32 v178, v118, v118
	v_add_f32_e32 v147, v147, v178
	v_add_f32_e32 v146, v146, v147
	v_mul_f32_e32 v147, v129, v129
	v_mul_f32_e32 v178, v131, v131
	v_fmac_f32_e32 v147, v128, v128
	v_fmac_f32_e32 v178, v130, v130
	v_add_f32_e32 v147, v147, v178
	v_add_f32_e32 v146, v146, v147
	ds_write_b32 v145, v146
	v_mul_f32_e32 v146, v113, v113
	v_mul_f32_e32 v147, v115, v115
	v_fmac_f32_e32 v146, v112, v112
	v_fmac_f32_e32 v147, v114, v114
	v_add_f32_e32 v146, v146, v147
	v_mul_f32_e32 v147, v105, v105
	v_mul_f32_e32 v178, v107, v107
	v_fmac_f32_e32 v147, v104, v104
	v_fmac_f32_e32 v178, v106, v106
	v_add_f32_e32 v147, v147, v178
	v_add_f32_e32 v146, v146, v147
	v_mul_f32_e32 v147, v101, v101
	v_mul_f32_e32 v178, v103, v103
	v_fmac_f32_e32 v147, v100, v100
	v_fmac_f32_e32 v178, v102, v102
	v_add_f32_e32 v147, v147, v178
	v_add_f32_e32 v146, v146, v147
	v_mul_f32_e32 v147, v109, v109
	v_mul_f32_e32 v178, v111, v111
	v_fmac_f32_e32 v147, v108, v108
	v_fmac_f32_e32 v178, v110, v110
	v_add_f32_e32 v147, v147, v178
	v_add_f32_e32 v146, v146, v147
	ds_write_b32 v145, v146 offset:1088
	v_mul_f32_e32 v146, v89, v89
	v_mul_f32_e32 v147, v91, v91
	v_fmac_f32_e32 v146, v88, v88
	v_fmac_f32_e32 v147, v90, v90
	v_add_f32_e32 v146, v146, v147
	v_mul_f32_e32 v147, v93, v93
	v_mul_f32_e32 v178, v95, v95
	v_fmac_f32_e32 v147, v92, v92
	v_fmac_f32_e32 v178, v94, v94
	v_add_f32_e32 v147, v147, v178
	v_add_f32_e32 v146, v146, v147
	v_mul_f32_e32 v147, v85, v85
	v_mul_f32_e32 v178, v87, v87
	v_fmac_f32_e32 v147, v84, v84
	v_fmac_f32_e32 v178, v86, v86
	v_add_f32_e32 v147, v147, v178
	v_add_f32_e32 v146, v146, v147
	v_mul_f32_e32 v147, v73, v73
	v_mul_f32_e32 v178, v75, v75
	v_fmac_f32_e32 v147, v72, v72
	v_fmac_f32_e32 v178, v74, v74
	v_add_f32_e32 v147, v147, v178
	v_add_f32_e32 v146, v146, v147
	ds_write_b32 v145, v146 offset:2176
	v_mul_f32_e32 v146, v81, v81
	v_mul_f32_e32 v147, v83, v83
	v_fmac_f32_e32 v146, v80, v80
	v_fmac_f32_e32 v147, v82, v82
	v_add_f32_e32 v146, v146, v147
	s_waitcnt vmcnt(4)
	v_pk_fma_f32 v[10:11], v[10:11], v[142:143], v[210:211]
	v_pk_fma_f32 v[8:9], v[8:9], v[140:141], v[208:209]
	global_store_dwordx4 v[34:35], v[8:11], off offset:64
	v_mul_f32_e32 v147, v77, v77
	v_mul_f32_e32 v178, v79, v79
	v_fmac_f32_e32 v147, v76, v76
	v_fmac_f32_e32 v178, v78, v78
	v_add_f32_e32 v147, v147, v178
	v_add_f32_e32 v146, v146, v147
	v_mul_f32_e32 v147, v69, v69
	v_mul_f32_e32 v178, v71, v71
	v_fmac_f32_e32 v147, v68, v68
	v_fmac_f32_e32 v178, v70, v70
	v_add_f32_e32 v147, v147, v178
	v_add_f32_e32 v146, v146, v147
	v_mul_f32_e32 v147, v65, v65
	v_mul_f32_e32 v178, v67, v67
	v_fmac_f32_e32 v147, v64, v64
	v_fmac_f32_e32 v178, v66, v66
	v_add_f32_e32 v147, v147, v178
	v_add_f32_e32 v146, v146, v147
	ds_write_b32 v145, v146 offset:3264
	v_mul_f32_e32 v146, v61, v61
	v_mul_f32_e32 v147, v63, v63
	v_fmac_f32_e32 v146, v60, v60
	v_fmac_f32_e32 v147, v62, v62
	v_add_f32_e32 v146, v146, v147
	v_mul_f32_e32 v147, v57, v57
	v_mul_f32_e32 v178, v59, v59
	v_fmac_f32_e32 v147, v56, v56
	v_fmac_f32_e32 v178, v58, v58
	v_add_f32_e32 v147, v147, v178
	v_add_u32_e32 v144, s1, v177
	s_movk_i32 s0, 0x100
	v_cmp_gt_i32_e64 s[4:5], s0, v144
	s_waitcnt vmcnt(4)
	v_pk_fma_f32 v[6:7], v[6:7], v[138:139], v[214:215]
	v_pk_fma_f32 v[4:5], v[4:5], v[136:137], v[212:213]
	global_store_dwordx4 v[34:35], v[4:7], off offset:512
	v_mul_f32_e32 v141, v53, v53
	v_mul_f32_e32 v142, v55, v55
	v_fmac_f32_e32 v141, v52, v52
	v_fmac_f32_e32 v142, v54, v54
	v_add_f32_e32 v140, v146, v147
	v_add_f32_e32 v141, v141, v142
	v_add_f32_e32 v140, v140, v141
	v_mul_f32_e32 v141, v41, v41
	v_mul_f32_e32 v142, v43, v43
	v_fmac_f32_e32 v141, v40, v40
	v_fmac_f32_e32 v142, v42, v42
	v_add_f32_e32 v141, v141, v142
	v_add_f32_e32 v140, v140, v141
	ds_write_b32 v145, v140 offset:8704
	v_mul_f32_e32 v140, v49, v49
	v_mul_f32_e32 v141, v51, v51
	v_fmac_f32_e32 v140, v48, v48
	v_fmac_f32_e32 v141, v50, v50
	v_add_f32_e32 v140, v140, v141
	v_mul_f32_e32 v141, v45, v45
	v_mul_f32_e32 v142, v47, v47
	v_fmac_f32_e32 v141, v44, v44
	v_fmac_f32_e32 v142, v46, v46
	v_add_f32_e32 v141, v141, v142
	v_add_f32_e32 v140, v140, v141
	v_mul_f32_e32 v141, v37, v37
	v_mul_f32_e32 v142, v39, v39
	v_fmac_f32_e32 v141, v36, v36
	v_fmac_f32_e32 v142, v38, v38
	v_add_f32_e32 v141, v141, v142
	v_add_f32_e32 v140, v140, v141
	v_mul_f32_e32 v141, v97, v97
	v_mul_f32_e32 v142, v99, v99
	v_fmac_f32_e32 v141, v96, v96
	v_fmac_f32_e32 v142, v98, v98
	v_add_f32_e32 v141, v141, v142
	v_add_f32_e32 v140, v140, v141
	ds_write_b32 v145, v140 offset:9792
	v_mul_f32_e32 v140, v25, v25
	v_mul_f32_e32 v141, v27, v27
	v_fmac_f32_e32 v140, v24, v24
	v_fmac_f32_e32 v141, v26, v26
	v_add_f32_e32 v140, v140, v141
	v_mul_f32_e32 v141, v29, v29
	v_mul_f32_e32 v142, v31, v31
	v_fmac_f32_e32 v141, v28, v28
	v_fmac_f32_e32 v142, v30, v30
	v_add_f32_e32 v141, v141, v142
	v_add_f32_e32 v140, v140, v141
	v_mul_f32_e32 v141, v21, v21
	v_mul_f32_e32 v142, v23, v23
	v_fmac_f32_e32 v141, v20, v20
	v_fmac_f32_e32 v142, v22, v22
	v_add_f32_e32 v141, v141, v142
	v_add_f32_e32 v140, v140, v141
	v_mul_f32_e32 v141, v13, v13
	v_mul_f32_e32 v142, v15, v15
	v_fmac_f32_e32 v141, v12, v12
	v_fmac_f32_e32 v142, v14, v14
	v_add_f32_e32 v141, v141, v142
	v_add_f32_e32 v140, v140, v141
	ds_write_b32 v145, v140 offset:10880
	v_mul_f32_e32 v140, v17, v17
	v_mul_f32_e32 v141, v19, v19
	v_fmac_f32_e32 v140, v16, v16
	v_fmac_f32_e32 v141, v18, v18
	v_add_f32_e32 v140, v140, v141
	v_mul_f32_e32 v141, v9, v9
	v_mul_f32_e32 v142, v11, v11
	v_fmac_f32_e32 v141, v8, v8
	v_fmac_f32_e32 v142, v10, v10
	v_add_f32_e32 v141, v141, v142
	v_add_f32_e32 v140, v140, v141
	v_mul_f32_e32 v141, v5, v5
	v_mul_f32_e32 v142, v7, v7
	v_fmac_f32_e32 v141, v4, v4
	v_fmac_f32_e32 v142, v6, v6
	v_add_f32_e32 v141, v141, v142
	v_add_f32_e32 v140, v140, v141
	s_waitcnt vmcnt(4)
	v_pk_fma_f32 v[2:3], v[2:3], v[134:135], v[218:219]
	v_pk_fma_f32 v[0:1], v[0:1], v[132:133], v[216:217]
	global_store_dwordx4 v[34:35], v[0:3], off offset:576
	v_mul_f32_e32 v34, v1, v1
	v_mul_f32_e32 v35, v3, v3
	v_fmac_f32_e32 v34, v0, v0
	v_fmac_f32_e32 v35, v2, v2
	v_add_f32_e32 v34, v34, v35
	v_add_f32_e32 v34, v140, v34
	ds_write_b32 v145, v34 offset:11968
	s_waitcnt lgkmcnt(0)
	s_barrier
	v_add_u32_e32 v34, s6, v144
	v_ashrrev_i32_e32 v35, 31, v34
	s_and_saveexec_b64 s[6:7], s[4:5]
	s_cbranch_execz .LBB0_909
	v_mul_lo_u32 v132, v144, s9
	v_add_u32_e32 v142, 0, v132
	ds_read2_b32 v[132:133], v142 offset1:1
	ds_read2_b32 v[134:135], v142 offset0:2 offset1:3
	ds_read2_b32 v[136:137], v142 offset0:4 offset1:5
	ds_read2_b32 v[138:139], v142 offset0:6 offset1:7
	ds_read2_b32 v[140:141], v142 offset0:8 offset1:9
	s_waitcnt lgkmcnt(4)
	v_add_f32_e32 v132, 0, v132
	v_add_f32_e32 v132, v132, v133
	s_waitcnt lgkmcnt(3)
	v_add_f32_e32 v132, v132, v134
	v_add_f32_e32 v132, v132, v135
	s_waitcnt lgkmcnt(2)
	v_add_f32_e32 v132, v132, v136
	v_add_f32_e32 v132, v132, v137
	s_waitcnt lgkmcnt(1)
	v_add_f32_e32 v132, v132, v138
	v_add_f32_e32 v138, v132, v139
	ds_read2_b32 v[132:133], v142 offset0:10 offset1:11
	ds_read2_b32 v[134:135], v142 offset0:12 offset1:13
	ds_read2_b32 v[136:137], v142 offset0:14 offset1:15
	s_waitcnt lgkmcnt(3)
	v_add_f32_e32 v138, v138, v140
	v_add_f32_e32 v138, v138, v141
	s_waitcnt lgkmcnt(2)
	v_add_f32_e32 v132, v138, v132
	v_add_f32_e32 v132, v132, v133
	s_waitcnt lgkmcnt(1)
	v_add_f32_e32 v132, v132, v134
	v_add_f32_e32 v132, v132, v135
	s_waitcnt lgkmcnt(0)
	v_add_f32_e32 v132, v132, v136
	v_add_f32_e32 v134, v132, v137
	v_lshlrev_b64 v[132:133], 5, v[34:35]
	v_lshl_add_u64 v[132:133], v[32:33], 0, v[132:133]
	s_ashr_i32 s11, s10, 31
	v_lshl_add_u64 v[132:133], s[10:11], 2, v[132:133]
	global_atomic_swap v[132:133], v134, off

.LBB0_1142:
	v_ashrrev_i32_e32 v128, 4, v193
	s_lshl_b32 s0, s14, 8
	v_lshlrev_b32_e32 v182, 2, v128
	s_or_b32 s0, s0, s63
	v_add_u32_e32 v166, s0, v182
	s_ashr_i32 s0, s30, 31
	s_lshr_b32 s0, s0, 29
	s_add_i32 s0, s30, s0
	s_lshl_b32 s15, s30, 8
	s_ashr_i32 s0, s0, 3
	s_mul_hi_i32 s7, s0, 0x3000
	s_mul_i32 s6, s0, 0x3000
	v_add_u32_e32 v144, s15, v192
	v_lshl_add_u64 v[170:171], s[6:7], 2, v[162:163]
	v_ashrrev_i32_e32 v167, 31, v166
	v_ashrrev_i32_e32 v145, 31, v144
	v_lshl_add_u64 v[128:129], v[166:167], 2, v[170:171]
	s_mov_b64 s[6:7], 0x40a000
	s_mov_b32 s0, 0x40a000
	v_lshlrev_b64 v[168:169], 11, v[144:145]
	v_lshl_add_u64 v[140:141], v[128:129], 0, s[6:7]
	v_add_co_u32_e32 v128, vcc, s0, v128
	v_lshl_add_u64 v[132:133], v[168:169], 0, v[166:167]
	s_nop 0
	v_addc_co_u32_e32 v129, vcc, 0, v129, vcc
	v_lshlrev_b64 v[158:159], 2, v[132:133]
	s_waitcnt vmcnt(0)
	s_barrier
	global_load_dwordx4 v[128:131], v[128:129], off
	v_lshl_add_u64 v[142:143], v[164:165], 0, v[158:159]
	global_load_dwordx4 v[208:211], v[142:143], off
	global_load_dwordx4 v[212:215], v[142:143], off offset:64
	global_load_dwordx4 v[136:139], v[140:141], off offset:64
	global_load_dwordx4 v[132:135], v[140:141], off offset:512
	global_load_dwordx4 v[216:219], v[142:143], off offset:512
	global_load_dwordx4 v[220:223], v[142:143], off offset:576
	global_load_dwordx4 v[140:143], v[140:141], off offset:576
	v_or_b32_e32 v172, 16, v144
	v_ashrrev_i32_e32 v173, 31, v172
	s_mov_b64 s[6:7], 0x2fc80000
	v_lshlrev_b64 v[172:173], 11, v[172:173]
	v_lshl_add_u64 v[186:187], v[162:163], 0, s[6:7]
	v_lshl_add_u64 v[178:179], v[172:173], 0, v[166:167]
	v_lshl_add_u64 v[158:159], v[186:187], 0, v[158:159]
	v_lshlrev_b64 v[180:181], 2, v[178:179]
	v_lshl_add_u64 v[178:179], v[164:165], 0, v[180:181]
	global_load_dwordx4 v[224:227], v[178:179], off
	global_load_dwordx4 v[228:231], v[178:179], off offset:64
	global_load_dwordx4 v[232:235], v[178:179], off offset:512
	global_load_dwordx4 v[236:239], v[178:179], off offset:576
	v_lshl_add_u64 v[180:181], v[186:187], 0, v[180:181]
	s_mov_b64 s[6:7], 0x40000
	s_mov_b64 s[8:9], 0x50000
	s_lshl_b32 s17, s62, 4
	s_movk_i32 s16, 0x44
	v_readlane_b32 s0, v254, 0
	s_mov_b64 s[10:11], 0x58000
	v_mul_lo_u32 v183, v192, s16
	v_add_u32_e32 v194, s0, v193
	s_add_i32 s0, s17, 0
	v_add3_u32 v195, s0, v182, v183
	v_lshl_add_u64 v[182:183], v[168:169], 0, s[10:11]
	v_lshl_add_u64 v[198:199], v[182:183], 0, v[166:167]
	v_lshlrev_b64 v[198:199], 2, v[198:199]
	s_movk_i32 s0, 0x100
	s_waitcnt vmcnt(8)
	v_pk_fma_f32 v[122:123], v[122:123], v[138:139], v[214:215]
	v_pk_fma_f32 v[120:121], v[120:121], v[136:137], v[212:213]
	v_pk_fma_f32 v[126:127], v[126:127], v[130:131], v[210:211]
	v_pk_fma_f32 v[124:125], v[124:125], v[128:129], v[208:209]
	s_waitcnt vmcnt(6)
	v_pk_fma_f32 v[118:119], v[118:119], v[134:135], v[218:219]
	v_pk_fma_f32 v[116:117], v[116:117], v[132:133], v[216:217]
	s_waitcnt vmcnt(4)
	v_pk_fma_f32 v[114:115], v[114:115], v[142:143], v[222:223]
	v_pk_fma_f32 v[112:113], v[112:113], v[140:141], v[220:221]
	global_store_dwordx4 v[158:159], v[124:127], off
	global_store_dwordx4 v[158:159], v[120:123], off offset:64
	global_store_dwordx4 v[158:159], v[116:119], off offset:512
	global_store_dwordx4 v[158:159], v[112:115], off offset:576
	v_or_b32_e32 v158, 32, v144
	v_ashrrev_i32_e32 v159, 31, v158
	v_lshlrev_b64 v[174:175], 11, v[158:159]
	v_lshl_add_u64 v[158:159], v[174:175], 0, v[166:167]
	v_lshlrev_b64 v[158:159], 2, v[158:159]
	v_lshl_add_u64 v[184:185], v[164:165], 0, v[158:159]
	global_load_dwordx4 v[240:243], v[184:185], off
	global_load_dwordx4 v[244:247], v[184:185], off offset:64
	global_load_dwordx4 v[248:251], v[184:185], off offset:512
	global_load_dwordx4 v[208:211], v[184:185], off offset:576
	v_or_b32_e32 v144, 48, v144
	v_ashrrev_i32_e32 v145, 31, v144
	v_mul_f32_e32 v202, v121, v121
	v_mul_f32_e32 v203, v123, v123
	v_mul_f32_e32 v204, v117, v117
	v_mul_f32_e32 v205, v119, v119
	v_fmac_f32_e32 v202, v120, v120
	v_fmac_f32_e32 v203, v122, v122
	v_mul_f32_e32 v206, v113, v113
	v_mul_f32_e32 v207, v115, v115
	v_fmac_f32_e32 v204, v116, v116
	v_fmac_f32_e32 v205, v118, v118
	v_fmac_f32_e32 v206, v112, v112
	v_fmac_f32_e32 v207, v114, v114
	s_waitcnt vmcnt(11)
	v_pk_fma_f32 v[110:111], v[110:111], v[130:131], v[226:227]
	v_pk_fma_f32 v[108:109], v[108:109], v[128:129], v[224:225]
	s_waitcnt vmcnt(10)
	v_pk_fma_f32 v[106:107], v[106:107], v[138:139], v[230:231]
	v_pk_fma_f32 v[104:105], v[104:105], v[136:137], v[228:229]
	s_waitcnt vmcnt(9)
	v_pk_fma_f32 v[102:103], v[102:103], v[134:135], v[234:235]
	v_pk_fma_f32 v[100:101], v[100:101], v[132:133], v[232:233]
	s_waitcnt vmcnt(8)
	v_pk_fma_f32 v[98:99], v[98:99], v[142:143], v[238:239]
	v_pk_fma_f32 v[96:97], v[96:97], v[140:141], v[236:237]
	global_store_dwordx4 v[180:181], v[108:111], off
	global_store_dwordx4 v[180:181], v[104:107], off offset:64
	global_store_dwordx4 v[180:181], v[100:103], off offset:512
	global_store_dwordx4 v[180:181], v[96:99], off offset:576
	v_lshlrev_b64 v[176:177], 11, v[144:145]
	v_lshl_add_u64 v[144:145], v[176:177], 0, v[166:167]
	v_lshlrev_b64 v[184:185], 2, v[144:145]
	v_lshl_add_u64 v[144:145], v[186:187], 0, v[158:159]
	v_lshl_add_u64 v[158:159], v[164:165], 0, v[184:185]
	global_load_dwordx4 v[212:215], v[158:159], off
	global_load_dwordx4 v[216:219], v[158:159], off offset:64
	global_load_dwordx4 v[220:223], v[158:159], off offset:512
	global_load_dwordx4 v[224:227], v[158:159], off offset:576
	s_waitcnt vmcnt(11)
	v_pk_fma_f32 v[94:95], v[94:95], v[130:131], v[242:243]
	v_pk_fma_f32 v[92:93], v[92:93], v[128:129], v[240:241]
	s_waitcnt vmcnt(10)
	v_pk_fma_f32 v[90:91], v[90:91], v[138:139], v[246:247]
	v_pk_fma_f32 v[88:89], v[88:89], v[136:137], v[244:245]
	s_waitcnt vmcnt(9)
	v_pk_fma_f32 v[86:87], v[86:87], v[134:135], v[250:251]
	v_pk_fma_f32 v[84:85], v[84:85], v[132:133], v[248:249]
	s_waitcnt vmcnt(8)
	v_pk_fma_f32 v[82:83], v[82:83], v[142:143], v[210:211]
	v_pk_fma_f32 v[80:81], v[80:81], v[140:141], v[208:209]
	global_store_dwordx4 v[144:145], v[92:95], off
	global_store_dwordx4 v[144:145], v[88:91], off offset:64
	global_store_dwordx4 v[144:145], v[84:87], off offset:512
	global_store_dwordx4 v[144:145], v[80:83], off offset:576
	v_lshl_add_u64 v[178:179], v[168:169], 0, s[6:7]
	v_lshl_add_u64 v[180:181], v[178:179], 0, v[166:167]
	v_lshlrev_b64 v[188:189], 2, v[180:181]
	v_lshl_add_u64 v[180:181], v[186:187], 0, v[184:185]
	v_lshl_add_u64 v[184:185], v[164:165], 0, v[188:189]
	global_load_dwordx4 v[228:231], v[184:185], off
	global_load_dwordx4 v[232:235], v[184:185], off offset:64
	global_load_dwordx4 v[236:239], v[184:185], off offset:512
	global_load_dwordx4 v[240:243], v[184:185], off offset:576
	s_mov_b64 s[6:7], 0x48000
	s_waitcnt vmcnt(11)
	v_pk_fma_f32 v[78:79], v[78:79], v[130:131], v[214:215]
	v_pk_fma_f32 v[76:77], v[76:77], v[128:129], v[212:213]
	s_waitcnt vmcnt(10)
	v_pk_fma_f32 v[74:75], v[74:75], v[138:139], v[218:219]
	v_pk_fma_f32 v[72:73], v[72:73], v[136:137], v[216:217]
	s_waitcnt vmcnt(9)
	v_pk_fma_f32 v[70:71], v[70:71], v[134:135], v[222:223]
	v_pk_fma_f32 v[68:69], v[68:69], v[132:133], v[220:221]
	s_waitcnt vmcnt(8)
	v_pk_fma_f32 v[66:67], v[66:67], v[142:143], v[226:227]
	v_pk_fma_f32 v[64:65], v[64:65], v[140:141], v[224:225]
	global_store_dwordx4 v[180:181], v[76:79], off
	global_store_dwordx4 v[180:181], v[72:75], off offset:64
	global_store_dwordx4 v[180:181], v[68:71], off offset:512
	global_store_dwordx4 v[180:181], v[64:67], off offset:576
	v_lshl_add_u64 v[180:181], v[168:169], 0, s[6:7]
	v_lshl_add_u64 v[184:185], v[180:181], 0, v[166:167]
	v_lshlrev_b64 v[190:191], 2, v[184:185]
	v_lshl_add_u64 v[184:185], v[186:187], 0, v[188:189]
	v_lshl_add_u64 v[188:189], v[164:165], 0, v[190:191]
	global_load_dwordx4 v[244:247], v[188:189], off
	global_load_dwordx4 v[248:251], v[188:189], off offset:64
	global_load_dwordx4 v[208:211], v[188:189], off offset:512
	global_load_dwordx4 v[212:215], v[188:189], off offset:576
	v_lshl_add_u64 v[190:191], v[186:187], 0, v[190:191]
	s_mov_b64 s[6:7], 0x80000
	s_waitcnt vmcnt(11)
	v_pk_fma_f32 v[62:63], v[62:63], v[130:131], v[230:231]
	v_pk_fma_f32 v[60:61], v[60:61], v[128:129], v[228:229]
	s_waitcnt vmcnt(10)
	v_pk_fma_f32 v[58:59], v[58:59], v[138:139], v[234:235]
	v_pk_fma_f32 v[56:57], v[56:57], v[136:137], v[232:233]
	s_waitcnt vmcnt(9)
	v_pk_fma_f32 v[54:55], v[54:55], v[134:135], v[238:239]
	v_pk_fma_f32 v[52:53], v[52:53], v[132:133], v[236:237]
	s_waitcnt vmcnt(8)
	v_pk_fma_f32 v[50:51], v[50:51], v[142:143], v[242:243]
	v_pk_fma_f32 v[48:49], v[48:49], v[140:141], v[240:241]
	global_store_dwordx4 v[184:185], v[60:63], off
	global_store_dwordx4 v[184:185], v[56:59], off offset:64
	global_store_dwordx4 v[184:185], v[52:55], off offset:512
	global_store_dwordx4 v[184:185], v[48:51], off offset:576
	v_lshl_add_u64 v[184:185], v[168:169], 0, s[8:9]
	v_lshl_add_u64 v[196:197], v[184:185], 0, v[166:167]
	v_lshlrev_b64 v[196:197], 2, v[196:197]
	v_lshl_add_u64 v[200:201], v[164:165], 0, v[196:197]
	global_load_dwordx4 v[216:219], v[200:201], off
	global_load_dwordx4 v[220:223], v[200:201], off offset:64
	global_load_dwordx4 v[224:227], v[200:201], off offset:512
	global_load_dwordx4 v[228:231], v[200:201], off offset:576
	v_lshl_add_u64 v[196:197], v[186:187], 0, v[196:197]
	v_lshl_add_u64 v[164:165], v[164:165], 0, v[198:199]
	global_load_dwordx4 v[232:235], v[164:165], off
	global_load_dwordx4 v[236:239], v[164:165], off offset:64
	global_load_dwordx4 v[240:243], v[164:165], off offset:512
	v_lshl_add_u64 v[186:187], v[186:187], 0, v[198:199]
	v_mul_f32_e32 v198, v125, v125
	v_mul_f32_e32 v199, v127, v127
	v_fmac_f32_e32 v198, v124, v124
	v_fmac_f32_e32 v199, v126, v126
	v_lshl_add_u64 v[188:189], v[162:163], 0, s[6:7]
	v_cmp_gt_i32_e64 s[6:7], s0, v194
	s_waitcnt vmcnt(14)
	v_pk_fma_f32 v[46:47], v[46:47], v[130:131], v[246:247]
	v_pk_fma_f32 v[44:45], v[44:45], v[128:129], v[244:245]
	global_load_dwordx4 v[244:247], v[164:165], off offset:576
	s_waitcnt vmcnt(14)
	v_pk_fma_f32 v[42:43], v[42:43], v[138:139], v[250:251]
	v_pk_fma_f32 v[40:41], v[40:41], v[136:137], v[248:249]
	s_waitcnt vmcnt(13)
	v_pk_fma_f32 v[38:39], v[38:39], v[134:135], v[210:211]
	v_pk_fma_f32 v[36:37], v[36:37], v[132:133], v[208:209]
	s_waitcnt vmcnt(12)
	v_pk_fma_f32 v[34:35], v[34:35], v[142:143], v[214:215]
	v_pk_fma_f32 v[32:33], v[32:33], v[140:141], v[212:213]
	global_store_dwordx4 v[190:191], v[44:47], off
	global_store_dwordx4 v[190:191], v[40:43], off offset:64
	global_store_dwordx4 v[190:191], v[36:39], off offset:512
	global_store_dwordx4 v[190:191], v[32:35], off offset:576
	v_add_f32_e32 v190, v198, v199
	v_add_f32_e32 v191, v202, v203
	v_add_f32_e32 v198, v204, v205
	v_add_f32_e32 v190, v190, v191
	v_add_f32_e32 v199, v206, v207
	v_add_f32_e32 v190, v190, v198
	v_add_f32_e32 v190, v190, v199
	ds_write_b32 v195, v190
	v_mul_f32_e32 v190, v109, v109
	v_mul_f32_e32 v191, v111, v111
	v_mul_f32_e32 v198, v105, v105
	v_mul_f32_e32 v199, v107, v107
	v_mul_f32_e32 v200, v101, v101
	v_mul_f32_e32 v201, v103, v103
	v_fmac_f32_e32 v190, v108, v108
	v_fmac_f32_e32 v191, v110, v110
	v_fmac_f32_e32 v198, v104, v104
	v_fmac_f32_e32 v199, v106, v106
	v_mul_f32_e32 v202, v97, v97
	v_mul_f32_e32 v203, v99, v99
	v_fmac_f32_e32 v200, v100, v100
	v_fmac_f32_e32 v201, v102, v102
	v_add_f32_e32 v190, v190, v191
	v_add_f32_e32 v191, v198, v199
	v_fmac_f32_e32 v202, v96, v96
	v_fmac_f32_e32 v203, v98, v98
	v_add_f32_e32 v198, v200, v201
	v_add_f32_e32 v190, v190, v191
	v_add_f32_e32 v199, v202, v203
	v_add_f32_e32 v190, v190, v198
	v_add_f32_e32 v190, v190, v199
	ds_write_b32 v195, v190 offset:1088
	v_mul_f32_e32 v190, v93, v93
	v_mul_f32_e32 v191, v95, v95
	v_mul_f32_e32 v198, v89, v89
	v_mul_f32_e32 v199, v91, v91
	v_mul_f32_e32 v200, v85, v85
	v_mul_f32_e32 v201, v87, v87
	v_fmac_f32_e32 v190, v92, v92
	v_fmac_f32_e32 v191, v94, v94
	v_fmac_f32_e32 v198, v88, v88
	v_fmac_f32_e32 v199, v90, v90
	v_mul_f32_e32 v202, v81, v81
	v_mul_f32_e32 v203, v83, v83
	v_fmac_f32_e32 v200, v84, v84
	v_fmac_f32_e32 v201, v86, v86
	v_add_f32_e32 v190, v190, v191
	v_add_f32_e32 v191, v198, v199
	v_fmac_f32_e32 v202, v80, v80
	v_fmac_f32_e32 v203, v82, v82
	v_add_f32_e32 v198, v200, v201
	v_add_f32_e32 v190, v190, v191
	v_add_f32_e32 v199, v202, v203
	v_add_f32_e32 v190, v190, v198
	v_add_f32_e32 v190, v190, v199
	ds_write_b32 v195, v190 offset:2176
	v_mul_f32_e32 v190, v77, v77
	v_mul_f32_e32 v191, v79, v79
	v_mul_f32_e32 v198, v73, v73
	v_mul_f32_e32 v199, v75, v75
	v_mul_f32_e32 v200, v69, v69
	v_mul_f32_e32 v201, v71, v71
	v_fmac_f32_e32 v190, v76, v76
	v_fmac_f32_e32 v191, v78, v78
	v_fmac_f32_e32 v198, v72, v72
	v_fmac_f32_e32 v199, v74, v74
	v_mul_f32_e32 v202, v65, v65
	v_mul_f32_e32 v203, v67, v67
	v_fmac_f32_e32 v200, v68, v68
	v_fmac_f32_e32 v201, v70, v70
	v_add_f32_e32 v190, v190, v191
	v_add_f32_e32 v191, v198, v199
	v_fmac_f32_e32 v202, v64, v64
	v_fmac_f32_e32 v203, v66, v66
	v_add_f32_e32 v198, v200, v201
	v_add_f32_e32 v199, v202, v203
	s_waitcnt vmcnt(11)
	v_pk_fma_f32 v[30:31], v[30:31], v[130:131], v[218:219]
	v_pk_fma_f32 v[28:29], v[28:29], v[128:129], v[216:217]
	s_waitcnt vmcnt(10)
	v_pk_fma_f32 v[26:27], v[26:27], v[138:139], v[222:223]
	v_pk_fma_f32 v[24:25], v[24:25], v[136:137], v[220:221]
	s_waitcnt vmcnt(9)
	v_pk_fma_f32 v[22:23], v[22:23], v[134:135], v[226:227]
	v_pk_fma_f32 v[20:21], v[20:21], v[132:133], v[224:225]
	s_waitcnt vmcnt(8)
	v_pk_fma_f32 v[18:19], v[18:19], v[142:143], v[230:231]
	v_pk_fma_f32 v[16:17], v[16:17], v[140:141], v[228:229]
	global_store_dwordx4 v[196:197], v[28:31], off
	global_store_dwordx4 v[196:197], v[24:27], off offset:64
	global_store_dwordx4 v[196:197], v[20:23], off offset:512
	global_store_dwordx4 v[196:197], v[16:19], off offset:576
	v_add_f32_e32 v152, v190, v191
	v_add_f32_e32 v156, v152, v198
	v_add_f32_e32 v190, v156, v199
	ds_write_b32 v195, v190 offset:3264
	v_mul_f32_e32 v164, v61, v61
	v_mul_f32_e32 v165, v63, v63
	v_mul_f32_e32 v190, v57, v57
	v_mul_f32_e32 v191, v59, v59
	v_mul_f32_e32 v196, v53, v53
	v_mul_f32_e32 v197, v55, v55
	v_fmac_f32_e32 v164, v60, v60
	v_fmac_f32_e32 v165, v62, v62
	v_fmac_f32_e32 v190, v56, v56
	v_fmac_f32_e32 v191, v58, v58
	v_mul_f32_e32 v198, v49, v49
	v_mul_f32_e32 v199, v51, v51
	v_fmac_f32_e32 v196, v52, v52
	v_fmac_f32_e32 v197, v54, v54
	v_add_f32_e32 v164, v164, v165
	v_add_f32_e32 v165, v190, v191
	v_fmac_f32_e32 v198, v48, v48
	v_fmac_f32_e32 v199, v50, v50
	v_add_f32_e32 v190, v196, v197
	v_add_f32_e32 v164, v164, v165
	v_add_f32_e32 v191, v198, v199
	v_add_f32_e32 v164, v164, v190
	v_add_f32_e32 v164, v164, v191
	ds_write_b32 v195, v164 offset:8704
	v_mul_f32_e32 v164, v45, v45
	v_mul_f32_e32 v165, v47, v47
	v_mul_f32_e32 v190, v41, v41
	v_mul_f32_e32 v191, v43, v43
	v_mul_f32_e32 v196, v37, v37
	v_mul_f32_e32 v197, v39, v39
	v_fmac_f32_e32 v164, v44, v44
	v_fmac_f32_e32 v165, v46, v46
	v_fmac_f32_e32 v190, v40, v40
	v_fmac_f32_e32 v191, v42, v42
	v_mul_f32_e32 v198, v33, v33
	v_mul_f32_e32 v199, v35, v35
	v_fmac_f32_e32 v196, v36, v36
	v_fmac_f32_e32 v197, v38, v38
	v_add_f32_e32 v164, v164, v165
	v_add_f32_e32 v165, v190, v191
	v_fmac_f32_e32 v198, v32, v32
	v_fmac_f32_e32 v199, v34, v34
	v_add_f32_e32 v190, v196, v197
	v_add_f32_e32 v164, v164, v165
	v_add_f32_e32 v191, v198, v199
	v_add_f32_e32 v164, v164, v190
	v_add_f32_e32 v164, v164, v191
	ds_write_b32 v195, v164 offset:9792
	v_mul_f32_e32 v164, v29, v29
	v_mul_f32_e32 v165, v31, v31
	v_mul_f32_e32 v190, v25, v25
	v_mul_f32_e32 v191, v27, v27
	v_mul_f32_e32 v196, v21, v21
	v_mul_f32_e32 v197, v23, v23
	v_fmac_f32_e32 v164, v28, v28
	v_fmac_f32_e32 v165, v30, v30
	v_fmac_f32_e32 v190, v24, v24
	v_fmac_f32_e32 v191, v26, v26
	v_mul_f32_e32 v198, v17, v17
	v_mul_f32_e32 v199, v19, v19
	v_fmac_f32_e32 v196, v20, v20
	v_fmac_f32_e32 v197, v22, v22
	v_add_f32_e32 v164, v164, v165
	v_add_f32_e32 v165, v190, v191
	v_fmac_f32_e32 v198, v16, v16
	v_fmac_f32_e32 v199, v18, v18
	v_add_f32_e32 v190, v196, v197
	v_add_f32_e32 v164, v164, v165
	v_add_f32_e32 v191, v198, v199
	v_add_f32_e32 v164, v164, v190
	v_add_f32_e32 v164, v164, v191
	ds_write_b32 v195, v164 offset:10880
	s_waitcnt vmcnt(11)
	v_pk_fma_f32 v[14:15], v[14:15], v[130:131], v[234:235]
	v_pk_fma_f32 v[12:13], v[12:13], v[128:129], v[232:233]
	s_waitcnt vmcnt(10)
	v_pk_fma_f32 v[10:11], v[10:11], v[138:139], v[238:239]
	v_pk_fma_f32 v[8:9], v[8:9], v[136:137], v[236:237]
	s_waitcnt vmcnt(9)
	v_pk_fma_f32 v[6:7], v[6:7], v[134:135], v[242:243]
	v_pk_fma_f32 v[4:5], v[4:5], v[132:133], v[240:241]
	v_mul_f32_e32 v128, v13, v13
	v_mul_f32_e32 v129, v15, v15
	v_mul_f32_e32 v130, v9, v9
	v_mul_f32_e32 v131, v11, v11
	s_waitcnt vmcnt(8)
	v_pk_fma_f32 v[2:3], v[2:3], v[142:143], v[246:247]
	v_pk_fma_f32 v[0:1], v[0:1], v[140:141], v[244:245]
	v_mul_f32_e32 v132, v5, v5
	v_mul_f32_e32 v133, v7, v7
	v_fmac_f32_e32 v128, v12, v12
	v_fmac_f32_e32 v129, v14, v14
	v_fmac_f32_e32 v130, v8, v8
	v_fmac_f32_e32 v131, v10, v10
	v_mul_f32_e32 v134, v1, v1
	v_mul_f32_e32 v135, v3, v3
	v_fmac_f32_e32 v132, v4, v4
	v_fmac_f32_e32 v133, v6, v6
	v_add_f32_e32 v128, v128, v129
	v_add_f32_e32 v129, v130, v131
	v_fmac_f32_e32 v134, v0, v0
	v_fmac_f32_e32 v135, v2, v2
	v_add_f32_e32 v130, v132, v133
	v_add_f32_e32 v128, v128, v129
	v_add_f32_e32 v131, v134, v135
	v_add_f32_e32 v128, v128, v130
	v_add_f32_e32 v128, v128, v131
	global_store_dwordx4 v[186:187], v[12:15], off
	global_store_dwordx4 v[186:187], v[8:11], off offset:64
	global_store_dwordx4 v[186:187], v[4:7], off offset:512
	global_store_dwordx4 v[186:187], v[0:3], off offset:576
	ds_write_b32 v195, v128 offset:11968
	s_waitcnt lgkmcnt(0)
	s_barrier
	v_add_u32_e32 v128, s15, v194
	v_ashrrev_i32_e32 v129, 31, v128
	s_and_saveexec_b64 s[8:9], s[6:7]
	s_cbranch_execz .LBB0_1144
	v_mul_lo_u32 v130, v194, s16
	v_add_u32_e32 v140, 0, v130
	ds_read2_b32 v[130:131], v140 offset1:1
	ds_read2_b32 v[132:133], v140 offset0:2 offset1:3
	ds_read2_b32 v[134:135], v140 offset0:4 offset1:5
	ds_read2_b32 v[136:137], v140 offset0:6 offset1:7
	ds_read2_b32 v[138:139], v140 offset0:8 offset1:9
	s_waitcnt lgkmcnt(4)
	v_add_f32_e32 v130, 0, v130
	v_add_f32_e32 v130, v130, v131
	s_waitcnt lgkmcnt(3)
	v_add_f32_e32 v130, v130, v132
	v_add_f32_e32 v130, v130, v133
	s_waitcnt lgkmcnt(2)
	v_add_f32_e32 v130, v130, v134
	v_add_f32_e32 v130, v130, v135
	s_waitcnt lgkmcnt(1)
	v_add_f32_e32 v130, v130, v136
	v_add_f32_e32 v136, v130, v137
	ds_read2_b32 v[130:131], v140 offset0:10 offset1:11
	ds_read2_b32 v[132:133], v140 offset0:12 offset1:13
	ds_read2_b32 v[134:135], v140 offset0:14 offset1:15
	s_waitcnt lgkmcnt(3)
	v_add_f32_e32 v136, v136, v138
	v_add_f32_e32 v136, v136, v139
	s_waitcnt lgkmcnt(2)
	v_add_f32_e32 v130, v136, v130
	v_add_f32_e32 v130, v130, v131
	s_waitcnt lgkmcnt(1)
	v_add_f32_e32 v130, v130, v132
	v_add_f32_e32 v130, v130, v133
	s_waitcnt lgkmcnt(0)
	v_add_f32_e32 v130, v130, v134
	v_add_f32_e32 v132, v130, v135
	v_lshlrev_b64 v[130:131], 5, v[128:129]
	v_lshl_add_u64 v[130:131], v[188:189], 0, v[130:131]
	s_ashr_i32 s15, s14, 31
	v_lshl_add_u64 v[130:131], s[14:15], 2, v[130:131]
	global_atomic_swap v[130:131], v132, off

.LBB0_1997:
	s_ashr_i32 s0, s36, 31
	s_lshr_b32 s0, s0, 29
	v_lshl_add_u32 v170, s36, 8, v158
	v_lshl_add_u32 v168, s64, 8, v160
	s_add_i32 s0, s36, s0
	v_ashrrev_i32_e32 v171, 31, v170
	s_ashr_i32 s0, s0, 3
	v_ashrrev_i32_e32 v169, 31, v168
	v_lshlrev_b64 v[130:131], 11, v[170:171]
	s_mul_hi_i32 s1, s0, 0xc000
	s_mul_i32 s0, s0, 0xc000
	v_lshl_add_u64 v[130:131], v[130:131], 0, v[168:169]
	s_add_u32 s0, s52, s0
	v_lshlrev_b64 v[156:157], 2, v[130:131]
	s_addc_u32 s1, s53, s1
	v_lshl_add_u64 v[172:173], s[12:13], 0, v[156:157]
	global_load_dwordx4 v[176:179], v[172:173], off
	v_lshl_add_u64 v[128:129], v[168:169], 2, s[0:1]
	global_load_dwordx4 v[140:143], v[128:129], off
	global_load_dwordx4 v[136:139], v[128:129], off offset:64
	global_load_dwordx4 v[132:135], v[128:129], off offset:512
	global_load_dwordx4 v[128:131], v[128:129], off offset:576
	global_load_dwordx4 v[180:183], v[172:173], off offset:64
	global_load_dwordx4 v[184:187], v[172:173], off offset:512
	global_load_dwordx4 v[188:191], v[172:173], off offset:576
	v_lshl_add_u64 v[174:175], s[6:7], 0, v[156:157]
	s_andn2_b64 vcc, exec, s[4:5]
	s_mov_b64 s[4:5], -1
	s_waitcnt vmcnt(6)
	v_pk_fma_f32 v[126:127], v[126:127], v[142:143], v[178:179]
	v_pk_fma_f32 v[124:125], v[124:125], v[140:141], v[176:177]
	global_store_dwordx4 v[174:175], v[124:127], off
	s_waitcnt vmcnt(3)
	v_pk_fma_f32 v[122:123], v[122:123], v[138:139], v[182:183]
	v_pk_fma_f32 v[120:121], v[120:121], v[136:137], v[180:181]
	global_store_dwordx4 v[174:175], v[120:123], off offset:64
	s_waitcnt vmcnt(3)
	v_pk_fma_f32 v[118:119], v[118:119], v[134:135], v[186:187]
	v_pk_fma_f32 v[116:117], v[116:117], v[132:133], v[184:185]
	global_store_dwordx4 v[174:175], v[116:119], off offset:512
	v_or_b32_e32 v120, 16, v170
	v_ashrrev_i32_e32 v121, 31, v120
	v_lshlrev_b64 v[120:121], 11, v[120:121]
	v_lshl_add_u64 v[120:121], v[120:121], 0, v[168:169]
	v_lshlrev_b64 v[120:121], 2, v[120:121]
	v_lshl_add_u64 v[122:123], s[12:13], 0, v[120:121]
	global_load_dwordx4 v[192:195], v[122:123], off
	global_load_dwordx4 v[196:199], v[122:123], off offset:64
	global_load_dwordx4 v[200:203], v[122:123], off offset:512
	global_load_dwordx4 v[204:207], v[122:123], off offset:576
	s_waitcnt vmcnt(7)
	v_pk_fma_f32 v[106:107], v[106:107], v[130:131], v[190:191]
	v_pk_fma_f32 v[104:105], v[104:105], v[128:129], v[188:189]
	global_store_dwordx4 v[174:175], v[104:107], off offset:576
	v_lshl_add_u64 v[116:117], s[6:7], 0, v[120:121]
	s_waitcnt vmcnt(4)
	v_pk_fma_f32 v[106:107], v[114:115], v[142:143], v[194:195]
	v_pk_fma_f32 v[104:105], v[112:113], v[140:141], v[192:193]
	global_store_dwordx4 v[116:117], v[104:107], off
	s_waitcnt vmcnt(4)
	s_nop 0
	v_pk_fma_f32 v[106:107], v[110:111], v[138:139], v[198:199]
	v_pk_fma_f32 v[104:105], v[108:109], v[136:137], v[196:197]
	global_store_dwordx4 v[116:117], v[104:107], off offset:64
	s_waitcnt vmcnt(4)
	v_pk_fma_f32 v[102:103], v[102:103], v[134:135], v[202:203]
	v_pk_fma_f32 v[100:101], v[100:101], v[132:133], v[200:201]
	global_store_dwordx4 v[116:117], v[100:103], off offset:512
	v_or_b32_e32 v104, 32, v170
	v_ashrrev_i32_e32 v105, 31, v104
	v_lshlrev_b64 v[104:105], 11, v[104:105]
	v_lshl_add_u64 v[104:105], v[104:105], 0, v[168:169]
	v_lshlrev_b64 v[104:105], 2, v[104:105]
	v_lshl_add_u64 v[106:107], s[12:13], 0, v[104:105]
	global_load_dwordx4 v[208:211], v[106:107], off
	global_load_dwordx4 v[212:215], v[106:107], off offset:64
	global_load_dwordx4 v[216:219], v[106:107], off offset:512
	global_load_dwordx4 v[220:223], v[106:107], off offset:576
	s_waitcnt vmcnt(8)
	v_pk_fma_f32 v[90:91], v[90:91], v[130:131], v[206:207]
	v_pk_fma_f32 v[88:89], v[88:89], v[128:129], v[204:205]
	global_store_dwordx4 v[116:117], v[88:91], off offset:576
	v_lshl_add_u64 v[100:101], s[6:7], 0, v[104:105]
	s_waitcnt vmcnt(4)
	v_pk_fma_f32 v[90:91], v[98:99], v[142:143], v[210:211]
	v_pk_fma_f32 v[88:89], v[96:97], v[140:141], v[208:209]
	global_store_dwordx4 v[100:101], v[88:91], off
	s_waitcnt vmcnt(4)
	s_nop 0
	v_pk_fma_f32 v[90:91], v[94:95], v[138:139], v[214:215]
	v_pk_fma_f32 v[88:89], v[92:93], v[136:137], v[212:213]
	global_store_dwordx4 v[100:101], v[88:91], off offset:64
	s_waitcnt vmcnt(4)
	v_pk_fma_f32 v[86:87], v[86:87], v[134:135], v[218:219]
	v_pk_fma_f32 v[84:85], v[84:85], v[132:133], v[216:217]
	global_store_dwordx4 v[100:101], v[84:87], off offset:512
	v_or_b32_e32 v88, 48, v170
	v_ashrrev_i32_e32 v89, 31, v88
	v_lshlrev_b64 v[88:89], 11, v[88:89]
	v_lshl_add_u64 v[88:89], v[88:89], 0, v[168:169]
	v_lshlrev_b64 v[88:89], 2, v[88:89]
	v_lshl_add_u64 v[90:91], s[12:13], 0, v[88:89]
	global_load_dwordx4 v[176:179], v[90:91], off
	global_load_dwordx4 v[180:183], v[90:91], off offset:64
	global_load_dwordx4 v[184:187], v[90:91], off offset:512
	global_load_dwordx4 v[188:191], v[90:91], off offset:576
	s_waitcnt vmcnt(8)
	v_pk_fma_f32 v[74:75], v[74:75], v[130:131], v[222:223]
	v_pk_fma_f32 v[72:73], v[72:73], v[128:129], v[220:221]
	global_store_dwordx4 v[100:101], v[72:75], off offset:576
	v_lshl_add_u64 v[84:85], s[6:7], 0, v[88:89]
	s_waitcnt vmcnt(4)
	v_pk_fma_f32 v[74:75], v[82:83], v[142:143], v[178:179]
	v_pk_fma_f32 v[72:73], v[80:81], v[140:141], v[176:177]
	global_store_dwordx4 v[84:85], v[72:75], off
	s_waitcnt vmcnt(4)
	s_nop 0
	v_pk_fma_f32 v[74:75], v[78:79], v[138:139], v[182:183]
	v_pk_fma_f32 v[72:73], v[76:77], v[136:137], v[180:181]
	global_store_dwordx4 v[84:85], v[72:75], off offset:64
	s_waitcnt vmcnt(4)
	v_pk_fma_f32 v[70:71], v[70:71], v[134:135], v[186:187]
	v_pk_fma_f32 v[68:69], v[68:69], v[132:133], v[184:185]
	global_store_dwordx4 v[84:85], v[68:71], off offset:512
	v_lshl_add_u64 v[72:73], v[156:157], 0, s[16:17]
	v_lshl_add_u64 v[74:75], s[12:13], 0, v[72:73]
	global_load_dwordx4 v[192:195], v[74:75], off
	global_load_dwordx4 v[196:199], v[74:75], off offset:64
	global_load_dwordx4 v[200:203], v[74:75], off offset:512
	global_load_dwordx4 v[204:207], v[74:75], off offset:576
	s_waitcnt vmcnt(8)
	v_pk_fma_f32 v[66:67], v[66:67], v[130:131], v[190:191]
	v_pk_fma_f32 v[64:65], v[64:65], v[128:129], v[188:189]
	global_store_dwordx4 v[84:85], v[64:67], off offset:576
	v_lshl_add_u64 v[68:69], s[6:7], 0, v[72:73]
	s_waitcnt vmcnt(4)
	v_pk_fma_f32 v[62:63], v[62:63], v[142:143], v[194:195]
	v_pk_fma_f32 v[60:61], v[60:61], v[140:141], v[192:193]
	global_store_dwordx4 v[68:69], v[60:63], off
	s_waitcnt vmcnt(4)
	v_pk_fma_f32 v[58:59], v[58:59], v[138:139], v[198:199]
	v_pk_fma_f32 v[56:57], v[56:57], v[136:137], v[196:197]
	global_store_dwordx4 v[68:69], v[56:59], off offset:64
	s_waitcnt vmcnt(4)
	v_pk_fma_f32 v[54:55], v[54:55], v[134:135], v[202:203]
	v_pk_fma_f32 v[52:53], v[52:53], v[132:133], v[200:201]
	global_store_dwordx4 v[68:69], v[52:55], off offset:512
	v_lshl_add_u64 v[56:57], v[156:157], 0, s[18:19]
	v_lshl_add_u64 v[58:59], s[12:13], 0, v[56:57]
	global_load_dwordx4 v[208:211], v[58:59], off
	global_load_dwordx4 v[212:215], v[58:59], off offset:64
	global_load_dwordx4 v[216:219], v[58:59], off offset:512
	global_load_dwordx4 v[220:223], v[58:59], off offset:576
	s_waitcnt vmcnt(8)
	v_pk_fma_f32 v[42:43], v[42:43], v[130:131], v[206:207]
	v_pk_fma_f32 v[40:41], v[40:41], v[128:129], v[204:205]
	global_store_dwordx4 v[68:69], v[40:43], off offset:576
	v_lshl_add_u64 v[52:53], s[6:7], 0, v[56:57]
	s_waitcnt vmcnt(4)
	v_pk_fma_f32 v[42:43], v[50:51], v[142:143], v[210:211]
	v_pk_fma_f32 v[40:41], v[48:49], v[140:141], v[208:209]
	global_store_dwordx4 v[52:53], v[40:43], off
	s_waitcnt vmcnt(4)
	s_nop 0
	v_pk_fma_f32 v[42:43], v[46:47], v[138:139], v[214:215]
	v_pk_fma_f32 v[40:41], v[44:45], v[136:137], v[212:213]
	global_store_dwordx4 v[52:53], v[40:43], off offset:64
	s_waitcnt vmcnt(4)
	v_pk_fma_f32 v[38:39], v[38:39], v[134:135], v[218:219]
	v_pk_fma_f32 v[36:37], v[36:37], v[132:133], v[216:217]
	global_store_dwordx4 v[52:53], v[36:39], off offset:512
	v_lshl_add_u64 v[40:41], v[156:157], 0, s[20:21]
	v_lshl_add_u64 v[42:43], s[12:13], 0, v[40:41]
	global_load_dwordx4 v[176:179], v[42:43], off
	global_load_dwordx4 v[180:183], v[42:43], off offset:64
	global_load_dwordx4 v[184:187], v[42:43], off offset:512
	global_load_dwordx4 v[188:191], v[42:43], off offset:576
	s_waitcnt vmcnt(8)
	v_pk_fma_f32 v[26:27], v[26:27], v[130:131], v[222:223]
	v_pk_fma_f32 v[24:25], v[24:25], v[128:129], v[220:221]
	global_store_dwordx4 v[52:53], v[24:27], off offset:576
	v_lshl_add_u64 v[36:37], s[6:7], 0, v[40:41]
	s_waitcnt vmcnt(4)
	v_pk_fma_f32 v[26:27], v[34:35], v[142:143], v[178:179]
	v_pk_fma_f32 v[24:25], v[32:33], v[140:141], v[176:177]
	global_store_dwordx4 v[36:37], v[24:27], off
	s_waitcnt vmcnt(4)
	s_nop 0
	v_pk_fma_f32 v[26:27], v[30:31], v[138:139], v[182:183]
	v_pk_fma_f32 v[24:25], v[28:29], v[136:137], v[180:181]
	global_store_dwordx4 v[36:37], v[24:27], off offset:64
	s_waitcnt vmcnt(4)
	v_pk_fma_f32 v[22:23], v[22:23], v[134:135], v[186:187]
	v_pk_fma_f32 v[20:21], v[20:21], v[132:133], v[184:185]
	global_store_dwordx4 v[36:37], v[20:23], off offset:512
	v_lshl_add_u64 v[24:25], v[156:157], 0, s[22:23]
	v_lshl_add_u64 v[26:27], s[12:13], 0, v[24:25]
	global_load_dwordx4 v[192:195], v[26:27], off
	global_load_dwordx4 v[196:199], v[26:27], off offset:64
	global_load_dwordx4 v[200:203], v[26:27], off offset:512
	global_load_dwordx4 v[204:207], v[26:27], off offset:576
	s_waitcnt vmcnt(8)
	v_pk_fma_f32 v[10:11], v[10:11], v[130:131], v[190:191]
	v_pk_fma_f32 v[8:9], v[8:9], v[128:129], v[188:189]
	global_store_dwordx4 v[36:37], v[8:11], off offset:576
	v_lshl_add_u64 v[20:21], s[6:7], 0, v[24:25]
	s_waitcnt vmcnt(4)
	v_pk_fma_f32 v[10:11], v[18:19], v[142:143], v[194:195]
	v_pk_fma_f32 v[8:9], v[16:17], v[140:141], v[192:193]
	global_store_dwordx4 v[20:21], v[8:11], off
	s_waitcnt vmcnt(4)
	s_nop 0
	v_pk_fma_f32 v[10:11], v[14:15], v[138:139], v[198:199]
	v_pk_fma_f32 v[8:9], v[12:13], v[136:137], v[196:197]
	global_store_dwordx4 v[20:21], v[8:11], off offset:64
	s_waitcnt vmcnt(4)
	v_pk_fma_f32 v[6:7], v[6:7], v[134:135], v[202:203]
	v_pk_fma_f32 v[4:5], v[4:5], v[132:133], v[200:201]
	global_store_dwordx4 v[20:21], v[4:7], off offset:512
	s_waitcnt vmcnt(4)
	v_pk_fma_f32 v[2:3], v[2:3], v[130:131], v[206:207]
	v_pk_fma_f32 v[0:1], v[0:1], v[128:129], v[204:205]
	global_store_dwordx4 v[20:21], v[0:3], off offset:576
	s_cbranch_vccnz .LBB0_1986
	s_andn2_b64 vcc, exec, s[10:11]
	s_cbranch_vccnz .LBB0_1985
	s_barrier
	s_branch .LBB0_1985
